# P4: VALU cndmask+cmp_ne mask negations replaced by one s_andn2_b64 each; the G<Q mask also rebuilt by v_cmp
# speedup vs baseline: 1.0080x; 1.0025x over previous
.LBB0_700:
	s_add_i32 s52, s47, -1
	s_bitcmp1_b32 s52, 0
	s_cselect_b32 s0, 0xa00, 0
	s_add_i32 s83, s0, 0
	v_mov_b32_e32 v70, s83
	ds_read_b32 v150, v70 offset:64512
	v_mov_b32_e32 v72, 0
	s_andn2_b64 s[88:89], exec, s[84:85]
	s_andn2_b64 vcc, exec, s[84:85]
	v_mov_b32_e32 v104, 0
	v_mov_b32_e32 v105, 0
	v_mov_b32_e32 v106, 0
	v_mov_b32_e32 v107, 0
	s_cbranch_vccnz .LBB0_702
	ds_read_b128 v[74:77], v191
	ds_read_b128 v[78:81], v191 offset:64
	ds_read_b128 v[202:205], v191 offset:128
	ds_read_b128 v[206:209], v191 offset:192
	s_waitcnt lgkmcnt(3)
	v_mfma_f32_16x16x32_f16 v[74:77], v[74:77], v[66:69], 0
	s_waitcnt lgkmcnt(2)
	v_mfma_f32_16x16x32_f16 v[74:77], v[78:81], v[46:49], v[74:77]
	s_waitcnt lgkmcnt(1)
	v_mfma_f32_16x16x32_f16 v[74:77], v[202:205], v[42:45], v[74:77]
	s_waitcnt lgkmcnt(0)
	v_mfma_f32_16x16x32_f16 v[104:107], v[206:209], v[38:41], v[74:77]

.LBB0_704:
	s_nop 4
	v_mov_b32_e32 v92, 0
	s_andn2_b64 s[90:91], exec, s[16:17]
	s_andn2_b64 vcc, exec, s[16:17]
	v_mov_b32_e32 v100, 0
	v_mov_b32_e32 v101, 0
	v_mov_b32_e32 v102, 0
	v_mov_b32_e32 v103, 0
	s_cbranch_vccnz .LBB0_706
	ds_read_b128 v[76:79], v191 offset:8704
	ds_read_b128 v[80:83], v191 offset:8768
	ds_read_b128 v[202:205], v191 offset:8832
	ds_read_b128 v[206:209], v191 offset:8896
	s_waitcnt lgkmcnt(3)
	v_mfma_f32_16x16x32_f16 v[76:79], v[76:79], v[66:69], 0
	s_waitcnt lgkmcnt(2)
	v_mfma_f32_16x16x32_f16 v[76:79], v[80:83], v[46:49], v[76:79]
	s_waitcnt lgkmcnt(1)
	v_mfma_f32_16x16x32_f16 v[76:79], v[202:205], v[42:45], v[76:79]
	s_waitcnt lgkmcnt(0)
	v_mfma_f32_16x16x32_f16 v[100:103], v[206:209], v[38:41], v[76:79]
.LBB0_706:
	s_andn2_b64 s[0:1], exec, s[18:19]
	s_andn2_b64 vcc, exec, s[18:19]
	v_mov_b32_e32 v93, 0
	v_mov_b32_e32 v94, 0
	v_mov_b32_e32 v95, 0
	s_cbranch_vccnz .LBB0_708
	ds_read_b128 v[76:79], v191 offset:13056
	ds_read_b128 v[80:83], v191 offset:13120
	ds_read_b128 v[202:205], v191 offset:13184
	ds_read_b128 v[206:209], v191 offset:13248
	s_waitcnt lgkmcnt(3)
	v_mfma_f32_16x16x32_f16 v[76:79], v[76:79], v[66:69], 0
	s_waitcnt lgkmcnt(2)
	v_mfma_f32_16x16x32_f16 v[76:79], v[80:83], v[46:49], v[76:79]
	s_waitcnt lgkmcnt(1)
	v_mfma_f32_16x16x32_f16 v[76:79], v[202:205], v[42:45], v[76:79]
	s_waitcnt lgkmcnt(0)
	v_mfma_f32_16x16x32_f16 v[92:95], v[206:209], v[38:41], v[76:79]
.LBB0_708:
	v_mov_b32_e32 v84, 0
	s_andn2_b64 s[92:93], exec, s[20:21]
	s_andn2_b64 vcc, exec, s[20:21]
	v_mov_b32_e32 v96, 0
	v_mov_b32_e32 v97, 0
	v_mov_b32_e32 v98, 0
	v_mov_b32_e32 v99, 0
	s_cbranch_vccnz .LBB0_710
	ds_read_b128 v[76:79], v191 offset:17408
	ds_read_b128 v[80:83], v191 offset:17472
	ds_read_b128 v[202:205], v191 offset:17536
	ds_read_b128 v[206:209], v191 offset:17600
	s_waitcnt lgkmcnt(3)
	v_mfma_f32_16x16x32_f16 v[76:79], v[76:79], v[66:69], 0
	s_waitcnt lgkmcnt(2)
	v_mfma_f32_16x16x32_f16 v[76:79], v[80:83], v[46:49], v[76:79]
	s_waitcnt lgkmcnt(1)
	v_mfma_f32_16x16x32_f16 v[76:79], v[202:205], v[42:45], v[76:79]
	s_waitcnt lgkmcnt(0)
	v_mfma_f32_16x16x32_f16 v[96:99], v[206:209], v[38:41], v[76:79]
.LBB0_710:
	s_andn2_b64 s[2:3], exec, s[22:23]
	s_andn2_b64 vcc, exec, s[22:23]
	v_mov_b32_e32 v85, 0
	v_mov_b32_e32 v86, 0
	v_mov_b32_e32 v87, 0
	s_cbranch_vccnz .LBB0_712
	ds_read_b128 v[76:79], v191 offset:21760
	ds_read_b128 v[80:83], v191 offset:21824
	ds_read_b128 v[202:205], v191 offset:21888
	ds_read_b128 v[206:209], v191 offset:21952
	s_waitcnt lgkmcnt(3)
	v_mfma_f32_16x16x32_f16 v[76:79], v[76:79], v[66:69], 0
	s_waitcnt lgkmcnt(2)
	v_mfma_f32_16x16x32_f16 v[76:79], v[80:83], v[46:49], v[76:79]
	s_waitcnt lgkmcnt(1)
	v_mfma_f32_16x16x32_f16 v[76:79], v[202:205], v[42:45], v[76:79]
	s_waitcnt lgkmcnt(0)
	v_mfma_f32_16x16x32_f16 v[84:87], v[206:209], v[38:41], v[76:79]
.LBB0_712:
	s_nop 3
	v_mov_b32_e32 v78, 0
	s_andn2_b64 s[94:95], exec, s[24:25]
	s_andn2_b64 vcc, exec, s[24:25]
	v_mov_b32_e32 v88, 0
	v_mov_b32_e32 v89, 0
	v_mov_b32_e32 v90, 0
	v_mov_b32_e32 v91, 0
	s_cbranch_vccnz .LBB0_714
	ds_read_b128 v[80:83], v191 offset:26112
	ds_read_b128 v[88:91], v191 offset:26176
	ds_read_b128 v[202:205], v191 offset:26240
	ds_read_b128 v[206:209], v191 offset:26304
	s_waitcnt lgkmcnt(3)
	v_mfma_f32_16x16x32_f16 v[80:83], v[80:83], v[66:69], 0
	s_waitcnt lgkmcnt(2)
	v_mfma_f32_16x16x32_f16 v[80:83], v[88:91], v[46:49], v[80:83]
	s_waitcnt lgkmcnt(1)
	v_mfma_f32_16x16x32_f16 v[80:83], v[202:205], v[42:45], v[80:83]
	s_waitcnt lgkmcnt(0)
	v_mfma_f32_16x16x32_f16 v[88:91], v[206:209], v[38:41], v[80:83]
.LBB0_714:
	s_andn2_b64 s[96:97], exec, s[26:27]
	s_andn2_b64 vcc, exec, s[26:27]
	v_mov_b32_e32 v79, 0
	s_nop 0
	v_mov_b32_e32 v80, 0
	v_mov_b32_e32 v81, 0
	s_cbranch_vccnz .LBB0_716
	ds_read_b128 v[76:79], v191 offset:30464
	ds_read_b128 v[80:83], v191 offset:30528
	ds_read_b128 v[202:205], v191 offset:30592
	ds_read_b128 v[206:209], v191 offset:30656
	s_waitcnt lgkmcnt(3)
	v_mfma_f32_16x16x32_f16 v[76:79], v[76:79], v[66:69], 0
	s_waitcnt lgkmcnt(2)
	v_mfma_f32_16x16x32_f16 v[76:79], v[80:83], v[46:49], v[76:79]
	s_waitcnt lgkmcnt(1)
	v_mfma_f32_16x16x32_f16 v[76:79], v[202:205], v[42:45], v[76:79]
	s_waitcnt lgkmcnt(0)
	v_mfma_f32_16x16x32_f16 v[78:81], v[206:209], v[38:41], v[76:79]
.LBB0_716:
	v_lshl_add_u32 v141, v151, 2, s83
	ds_read_b32 v143, v141 offset:62720
	v_lshl_add_u32 v196, v122, 2, s83
	s_mov_b64 s[38:39], -1
	s_and_b64 vcc, exec, s[84:85]
	s_cbranch_vccz .LBB0_733
	ds_read_b128 v[198:201], v196 offset:62208
	v_cmp_gt_i32_e64 s[38:39], 0, v244
	s_waitcnt lgkmcnt(0)
	v_sub_f32_e32 v70, v198, v143
	v_mul_f32_e32 v70, 0x3fb8aa3b, v70
	v_sub_f32_e32 v71, v199, v143
	v_exp_f32_e32 v70, v70
	v_mul_f32_e32 v71, 0x3fb8aa3b, v71
	v_exp_f32_e32 v71, v71
	v_sub_f32_e32 v76, v200, v143
	v_mul_f32_e32 v76, 0x3fb8aa3b, v76
	v_fma_mixlo_f16 v70, v104, v70, 0
	v_exp_f32_e32 v76, v76
	v_sub_f32_e32 v77, v201, v143
	v_cndmask_b32_e64 v70, v70, 0, s[38:39]
	v_mul_f32_e32 v77, 0x3fb8aa3b, v77
	v_fma_mixlo_f16 v71, v105, v71, 0
	v_cmp_lt_i32_e64 s[38:39], 0, v244
	v_exp_f32_e32 v77, v77
	s_nop 0
	v_cndmask_b32_e64 v71, 0, v71, s[38:39]
	v_pack_b32_f16 v70, v70, v71
	v_fma_mixlo_f16 v71, v106, v76, 0
	v_cmp_gt_i32_e64 s[38:39], 2, v244
	v_fma_mixlo_f16 v76, v107, v77, 0
	s_nop 0
	v_cndmask_b32_e64 v71, v71, 0, s[38:39]
	v_cmp_gt_i32_e64 s[38:39], 3, v244
	s_nop 1
	v_cndmask_b32_e64 v76, v76, 0, s[38:39]
	v_pack_b32_f16 v71, v71, v76
	s_cbranch_execz .LBB0_734

.LBB0_2100:
	s_add_i32 s56, s52, -1
	s_bitcmp1_b32 s56, 0
	s_cselect_b32 s0, 0xa00, 0
	s_add_i32 s9, s0, 0
	v_mov_b32_e32 v70, s9
	ds_read_b32 v146, v70 offset:64512
	v_mov_b32_e32 v72, 0
	s_andn2_b64 s[88:89], exec, s[82:83]
	s_andn2_b64 vcc, exec, s[82:83]
	v_mov_b32_e32 v100, 0
	v_mov_b32_e32 v101, 0
	v_mov_b32_e32 v102, 0
	v_mov_b32_e32 v103, 0
	s_cbranch_vccnz .LBB0_2102
	ds_read_b128 v[74:77], v187
	ds_read_b128 v[78:81], v187 offset:64
	ds_read_b128 v[202:205], v187 offset:128
	ds_read_b128 v[206:209], v187 offset:192
	s_waitcnt lgkmcnt(3)
	v_mfma_f32_16x16x32_f16 v[74:77], v[74:77], v[66:69], 0
	s_waitcnt lgkmcnt(2)
	v_mfma_f32_16x16x32_f16 v[74:77], v[78:81], v[46:49], v[74:77]
	s_waitcnt lgkmcnt(1)
	v_mfma_f32_16x16x32_f16 v[74:77], v[202:205], v[42:45], v[74:77]
	s_waitcnt lgkmcnt(0)
	v_mfma_f32_16x16x32_f16 v[100:103], v[206:209], v[38:41], v[74:77]

.LBB0_2104:
	s_nop 4
	v_mov_b32_e32 v76, 0
	s_andn2_b64 s[90:91], exec, s[16:17]
	s_andn2_b64 vcc, exec, s[16:17]
	v_mov_b32_e32 v96, 0
	v_mov_b32_e32 v97, 0
	v_mov_b32_e32 v98, 0
	v_mov_b32_e32 v99, 0
	s_cbranch_vccnz .LBB0_2106
	ds_read_b128 v[78:81], v187 offset:8704
	ds_read_b128 v[82:85], v187 offset:8768
	ds_read_b128 v[202:205], v187 offset:8832
	ds_read_b128 v[206:209], v187 offset:8896
	s_waitcnt lgkmcnt(3)
	v_mfma_f32_16x16x32_f16 v[78:81], v[78:81], v[66:69], 0
	s_waitcnt lgkmcnt(2)
	v_mfma_f32_16x16x32_f16 v[78:81], v[82:85], v[46:49], v[78:81]
	s_waitcnt lgkmcnt(1)
	v_mfma_f32_16x16x32_f16 v[78:81], v[202:205], v[42:45], v[78:81]
	s_waitcnt lgkmcnt(0)
	v_mfma_f32_16x16x32_f16 v[96:99], v[206:209], v[38:41], v[78:81]
.LBB0_2106:
	s_andn2_b64 s[0:1], exec, s[18:19]
	s_andn2_b64 vcc, exec, s[18:19]
	v_mov_b32_e32 v77, 0
	s_nop 0
	v_mov_b32_e32 v78, 0
	v_mov_b32_e32 v79, 0
	s_cbranch_vccnz .LBB0_2108
	ds_read_b128 v[76:79], v187 offset:13056
	ds_read_b128 v[80:83], v187 offset:13120
	ds_read_b128 v[202:205], v187 offset:13184
	ds_read_b128 v[206:209], v187 offset:13248
	s_waitcnt lgkmcnt(3)
	v_mfma_f32_16x16x32_f16 v[76:79], v[76:79], v[66:69], 0
	s_waitcnt lgkmcnt(2)
	v_mfma_f32_16x16x32_f16 v[76:79], v[80:83], v[46:49], v[76:79]
	s_waitcnt lgkmcnt(1)
	v_mfma_f32_16x16x32_f16 v[76:79], v[202:205], v[42:45], v[76:79]
	s_waitcnt lgkmcnt(0)
	v_mfma_f32_16x16x32_f16 v[76:79], v[206:209], v[38:41], v[76:79]
.LBB0_2108:
	v_mov_b32_e32 v80, 0
	s_andn2_b64 s[92:93], exec, s[20:21]
	s_andn2_b64 vcc, exec, s[20:21]
	v_mov_b32_e32 v92, 0
	v_mov_b32_e32 v93, 0
	v_mov_b32_e32 v94, 0
	v_mov_b32_e32 v95, 0
	s_cbranch_vccnz .LBB0_2110
	ds_read_b128 v[82:85], v187 offset:17408
	ds_read_b128 v[86:89], v187 offset:17472
	ds_read_b128 v[202:205], v187 offset:17536
	ds_read_b128 v[206:209], v187 offset:17600
	s_waitcnt lgkmcnt(3)
	v_mfma_f32_16x16x32_f16 v[82:85], v[82:85], v[66:69], 0
	s_waitcnt lgkmcnt(2)
	v_mfma_f32_16x16x32_f16 v[82:85], v[86:89], v[46:49], v[82:85]
	s_waitcnt lgkmcnt(1)
	v_mfma_f32_16x16x32_f16 v[82:85], v[202:205], v[42:45], v[82:85]
	s_waitcnt lgkmcnt(0)
	v_mfma_f32_16x16x32_f16 v[92:95], v[206:209], v[38:41], v[82:85]
.LBB0_2110:
	s_andn2_b64 s[2:3], exec, s[22:23]
	s_andn2_b64 vcc, exec, s[22:23]
	v_mov_b32_e32 v81, 0
	s_nop 0
	v_mov_b32_e32 v82, 0
	v_mov_b32_e32 v83, 0
	s_cbranch_vccnz .LBB0_2112
	ds_read_b128 v[80:83], v187 offset:21760
	ds_read_b128 v[84:87], v187 offset:21824
	ds_read_b128 v[202:205], v187 offset:21888
	ds_read_b128 v[206:209], v187 offset:21952
	s_waitcnt lgkmcnt(3)
	v_mfma_f32_16x16x32_f16 v[80:83], v[80:83], v[66:69], 0
	s_waitcnt lgkmcnt(2)
	v_mfma_f32_16x16x32_f16 v[80:83], v[84:87], v[46:49], v[80:83]
	s_waitcnt lgkmcnt(1)
	v_mfma_f32_16x16x32_f16 v[80:83], v[202:205], v[42:45], v[80:83]
	s_waitcnt lgkmcnt(0)
	v_mfma_f32_16x16x32_f16 v[80:83], v[206:209], v[38:41], v[80:83]
.LBB0_2112:
	v_mov_b32_e32 v84, 0
	s_andn2_b64 s[94:95], exec, s[24:25]
	s_andn2_b64 vcc, exec, s[24:25]
	v_mov_b32_e32 v88, 0
	v_mov_b32_e32 v89, 0
	v_mov_b32_e32 v90, 0
	v_mov_b32_e32 v91, 0
	s_cbranch_vccnz .LBB0_2114
	ds_read_b128 v[86:89], v187 offset:26112
	ds_read_b128 v[192:195], v187 offset:26176
	ds_read_b128 v[202:205], v187 offset:26240
	ds_read_b128 v[206:209], v187 offset:26304
	s_waitcnt lgkmcnt(3)
	v_mfma_f32_16x16x32_f16 v[86:89], v[86:89], v[66:69], 0
	s_waitcnt lgkmcnt(2)
	v_mfma_f32_16x16x32_f16 v[86:89], v[192:195], v[46:49], v[86:89]
	s_waitcnt lgkmcnt(1)
	v_mfma_f32_16x16x32_f16 v[86:89], v[202:205], v[42:45], v[86:89]
	s_waitcnt lgkmcnt(0)
	v_mfma_f32_16x16x32_f16 v[88:91], v[206:209], v[38:41], v[86:89]
.LBB0_2114:
	s_andn2_b64 s[96:97], exec, s[26:27]
	s_andn2_b64 vcc, exec, s[26:27]
	v_mov_b32_e32 v85, 0
	s_nop 0
	v_mov_b32_e32 v86, 0
	v_mov_b32_e32 v87, 0
	s_cbranch_vccnz .LBB0_2116
	ds_read_b128 v[84:87], v187 offset:30464
	ds_read_b128 v[192:195], v187 offset:30528
	ds_read_b128 v[202:205], v187 offset:30592
	ds_read_b128 v[206:209], v187 offset:30656
	s_waitcnt lgkmcnt(3)
	v_mfma_f32_16x16x32_f16 v[84:87], v[84:87], v[66:69], 0
	s_waitcnt lgkmcnt(2)
	v_mfma_f32_16x16x32_f16 v[84:87], v[192:195], v[46:49], v[84:87]
	s_waitcnt lgkmcnt(1)
	v_mfma_f32_16x16x32_f16 v[84:87], v[202:205], v[42:45], v[84:87]
	s_waitcnt lgkmcnt(0)
	v_mfma_f32_16x16x32_f16 v[84:87], v[206:209], v[38:41], v[84:87]
.LBB0_2116:
	v_lshl_add_u32 v137, v147, 2, s9
	ds_read_b32 v139, v137 offset:62720
	v_lshl_add_u32 v192, v118, 2, s9
	s_mov_b64 s[38:39], -1
	s_and_b64 vcc, exec, s[82:83]
	s_cbranch_vccz .LBB0_2133
	ds_read_b128 v[194:197], v192 offset:62208
	v_cmp_gt_i32_e64 s[12:13], 0, v244
	s_waitcnt lgkmcnt(0)
	v_sub_f32_e32 v70, v194, v139
	v_sub_f32_e32 v71, v195, v139
	v_mul_f32_e32 v70, 0x3fb8aa3b, v70
	v_mul_f32_e32 v71, 0x3fb8aa3b, v71
	v_exp_f32_e32 v70, v70
	v_exp_f32_e32 v71, v71
	v_sub_f32_e32 v193, v196, v139
	v_mul_f32_e32 v193, 0x3fb8aa3b, v193
	v_fma_mixlo_f16 v70, v100, v70, 0
	v_fma_mixlo_f16 v71, v101, v71, 0
	v_exp_f32_e32 v100, v193
	v_sub_f32_e32 v101, v197, v139
	v_cndmask_b32_e64 v70, v70, 0, s[12:13]
	v_mul_f32_e32 v101, 0x3fb8aa3b, v101
	v_cmp_lt_i32_e64 s[12:13], 0, v244
	v_exp_f32_e32 v101, v101
	s_nop 0
	v_cndmask_b32_e64 v71, 0, v71, s[12:13]
	v_pack_b32_f16 v70, v70, v71
	v_fma_mixlo_f16 v71, v102, v100, 0
	v_cmp_gt_i32_e64 s[12:13], 2, v244
	v_fma_mixlo_f16 v100, v103, v101, 0
	s_nop 0
	v_cndmask_b32_e64 v71, v71, 0, s[12:13]
	v_cmp_gt_i32_e64 s[12:13], 3, v244
	s_nop 1
	v_cndmask_b32_e64 v100, v100, 0, s[12:13]
	v_pack_b32_f16 v71, v71, v100
	s_cbranch_execz .LBB0_2134

.LBB0_3717:
	s_add_i32 s54, s49, -1
	s_bitcmp1_b32 s54, 0
	s_cselect_b32 s0, 0xa00, 0
	s_add_i32 s83, s0, 0
	v_mov_b32_e32 v70, s83
	ds_read_b32 v146, v70 offset:64512
	v_mov_b32_e32 v72, 0
	s_andn2_b64 s[88:89], exec, s[84:85]
	s_andn2_b64 vcc, exec, s[84:85]
	v_mov_b32_e32 v100, 0
	v_mov_b32_e32 v101, 0
	v_mov_b32_e32 v102, 0
	v_mov_b32_e32 v103, 0
	s_cbranch_vccnz .LBB0_3719
	ds_read_b128 v[74:77], v187
	ds_read_b128 v[78:81], v187 offset:64
	ds_read_b128 v[202:205], v187 offset:128
	ds_read_b128 v[206:209], v187 offset:192
	s_waitcnt lgkmcnt(3)
	v_mfma_f32_16x16x32_f16 v[74:77], v[74:77], v[66:69], 0
	s_waitcnt lgkmcnt(2)
	v_mfma_f32_16x16x32_f16 v[74:77], v[78:81], v[46:49], v[74:77]
	s_waitcnt lgkmcnt(1)
	v_mfma_f32_16x16x32_f16 v[74:77], v[202:205], v[42:45], v[74:77]
	s_waitcnt lgkmcnt(0)
	v_mfma_f32_16x16x32_f16 v[100:103], v[206:209], v[38:41], v[74:77]

.LBB0_3723:
	s_andn2_b64 s[80:81], exec, s[18:19]
	s_andn2_b64 vcc, exec, s[18:19]
	v_mov_b32_e32 v77, 0
	s_nop 0
	v_mov_b32_e32 v78, 0
	v_mov_b32_e32 v79, 0
	s_cbranch_vccnz .LBB0_3725
	ds_read_b128 v[76:79], v187 offset:13056
	ds_read_b128 v[80:83], v187 offset:13120
	ds_read_b128 v[202:205], v187 offset:13184
	ds_read_b128 v[206:209], v187 offset:13248
	s_waitcnt lgkmcnt(3)
	v_mfma_f32_16x16x32_f16 v[76:79], v[76:79], v[66:69], 0
	s_waitcnt lgkmcnt(2)
	v_mfma_f32_16x16x32_f16 v[76:79], v[80:83], v[46:49], v[76:79]
	s_waitcnt lgkmcnt(1)
	v_mfma_f32_16x16x32_f16 v[76:79], v[202:205], v[42:45], v[76:79]
	s_waitcnt lgkmcnt(0)
	v_mfma_f32_16x16x32_f16 v[76:79], v[206:209], v[38:41], v[76:79]

.LBB0_3733:
	v_lshl_add_u32 v137, v147, 2, s83
	ds_read_b32 v139, v137 offset:62720
	v_lshl_add_u32 v192, v118, 2, s83
	s_mov_b64 s[38:39], -1
	s_and_b64 vcc, exec, s[84:85]
	s_cbranch_vccz .LBB0_3750
	ds_read_b128 v[194:197], v192 offset:62208
	v_cmp_gt_i32_e64 s[38:39], 0, v244
	s_waitcnt lgkmcnt(0)
	v_sub_f32_e32 v70, v194, v139
	v_sub_f32_e32 v71, v195, v139
	v_mul_f32_e32 v70, 0x3fb8aa3b, v70
	v_mul_f32_e32 v71, 0x3fb8aa3b, v71
	v_exp_f32_e32 v70, v70
	v_exp_f32_e32 v71, v71
	v_sub_f32_e32 v193, v196, v139
	v_mul_f32_e32 v193, 0x3fb8aa3b, v193
	v_fma_mixlo_f16 v70, v100, v70, 0
	v_fma_mixlo_f16 v71, v101, v71, 0
	v_exp_f32_e32 v100, v193
	v_sub_f32_e32 v101, v197, v139
	v_cndmask_b32_e64 v70, v70, 0, s[38:39]
	v_mul_f32_e32 v101, 0x3fb8aa3b, v101
	v_cmp_lt_i32_e64 s[38:39], 0, v244
	v_exp_f32_e32 v101, v101
	s_nop 0
	v_cndmask_b32_e64 v71, 0, v71, s[38:39]
	v_pack_b32_f16 v70, v70, v71
	v_fma_mixlo_f16 v71, v102, v100, 0
	v_cmp_gt_i32_e64 s[38:39], 2, v244
	v_fma_mixlo_f16 v100, v103, v101, 0
	s_nop 0
	v_cndmask_b32_e64 v71, v71, 0, s[38:39]
	v_cmp_gt_i32_e64 s[38:39], 3, v244
	s_nop 1
	v_cndmask_b32_e64 v100, v100, 0, s[38:39]
	v_pack_b32_f16 v71, v71, v100
	s_cbranch_execz .LBB0_3751

.LBB0_5080:
	s_add_i32 s52, s47, -1
	s_bitcmp1_b32 s52, 0
	s_cselect_b32 s2, 0xa00, 0
	s_add_i32 s81, s2, 0
	v_mov_b32_e32 v70, s81
	ds_read_b32 v146, v70 offset:64512
	v_mov_b32_e32 v72, 0
	s_andn2_b64 s[86:87], exec, s[82:83]
	s_andn2_b64 vcc, exec, s[82:83]
	v_mov_b32_e32 v100, 0
	v_mov_b32_e32 v101, 0
	v_mov_b32_e32 v102, 0
	v_mov_b32_e32 v103, 0
	s_cbranch_vccnz .LBB0_5082
	ds_read_b128 v[74:77], v187
	ds_read_b128 v[78:81], v187 offset:64
	ds_read_b128 v[202:205], v187 offset:128
	ds_read_b128 v[206:209], v187 offset:192
	s_waitcnt lgkmcnt(3)
	v_mfma_f32_16x16x32_f16 v[74:77], v[74:77], v[66:69], 0
	s_waitcnt lgkmcnt(2)
	v_mfma_f32_16x16x32_f16 v[74:77], v[78:81], v[46:49], v[74:77]
	s_waitcnt lgkmcnt(1)
	v_mfma_f32_16x16x32_f16 v[74:77], v[202:205], v[42:45], v[74:77]
	s_waitcnt lgkmcnt(0)
	v_mfma_f32_16x16x32_f16 v[100:103], v[206:209], v[38:41], v[74:77]

.LBB0_5084:
	s_nop 4
	v_mov_b32_e32 v76, 0
	s_andn2_b64 s[88:89], exec, s[14:15]
	s_andn2_b64 vcc, exec, s[14:15]
	v_mov_b32_e32 v96, 0
	v_mov_b32_e32 v97, 0
	v_mov_b32_e32 v98, 0
	v_mov_b32_e32 v99, 0
	s_cbranch_vccnz .LBB0_5086
	ds_read_b128 v[78:81], v187 offset:8704
	ds_read_b128 v[82:85], v187 offset:8768
	ds_read_b128 v[202:205], v187 offset:8832
	ds_read_b128 v[206:209], v187 offset:8896
	s_waitcnt lgkmcnt(3)
	v_mfma_f32_16x16x32_f16 v[78:81], v[78:81], v[66:69], 0
	s_waitcnt lgkmcnt(2)
	v_mfma_f32_16x16x32_f16 v[78:81], v[82:85], v[46:49], v[78:81]
	s_waitcnt lgkmcnt(1)
	v_mfma_f32_16x16x32_f16 v[78:81], v[202:205], v[42:45], v[78:81]
	s_waitcnt lgkmcnt(0)
	v_mfma_f32_16x16x32_f16 v[96:99], v[206:209], v[38:41], v[78:81]
.LBB0_5086:
	s_andn2_b64 s[2:3], exec, s[16:17]
	s_andn2_b64 vcc, exec, s[16:17]
	v_mov_b32_e32 v77, 0
	s_nop 0
	v_mov_b32_e32 v78, 0
	v_mov_b32_e32 v79, 0
	s_cbranch_vccnz .LBB0_5088
	ds_read_b128 v[76:79], v187 offset:13056
	ds_read_b128 v[80:83], v187 offset:13120
	ds_read_b128 v[202:205], v187 offset:13184
	ds_read_b128 v[206:209], v187 offset:13248
	s_waitcnt lgkmcnt(3)
	v_mfma_f32_16x16x32_f16 v[76:79], v[76:79], v[66:69], 0
	s_waitcnt lgkmcnt(2)
	v_mfma_f32_16x16x32_f16 v[76:79], v[80:83], v[46:49], v[76:79]
	s_waitcnt lgkmcnt(1)
	v_mfma_f32_16x16x32_f16 v[76:79], v[202:205], v[42:45], v[76:79]
	s_waitcnt lgkmcnt(0)
	v_mfma_f32_16x16x32_f16 v[76:79], v[206:209], v[38:41], v[76:79]
.LBB0_5088:
	v_mov_b32_e32 v80, 0
	s_andn2_b64 s[90:91], exec, s[18:19]
	s_andn2_b64 vcc, exec, s[18:19]
	v_mov_b32_e32 v92, 0
	v_mov_b32_e32 v93, 0
	v_mov_b32_e32 v94, 0
	v_mov_b32_e32 v95, 0
	s_cbranch_vccnz .LBB0_5090
	ds_read_b128 v[82:85], v187 offset:17408
	ds_read_b128 v[86:89], v187 offset:17472
	ds_read_b128 v[202:205], v187 offset:17536
	ds_read_b128 v[206:209], v187 offset:17600
	s_waitcnt lgkmcnt(3)
	v_mfma_f32_16x16x32_f16 v[82:85], v[82:85], v[66:69], 0
	s_waitcnt lgkmcnt(2)
	v_mfma_f32_16x16x32_f16 v[82:85], v[86:89], v[46:49], v[82:85]
	s_waitcnt lgkmcnt(1)
	v_mfma_f32_16x16x32_f16 v[82:85], v[202:205], v[42:45], v[82:85]
	s_waitcnt lgkmcnt(0)
	v_mfma_f32_16x16x32_f16 v[92:95], v[206:209], v[38:41], v[82:85]
.LBB0_5090:
	s_andn2_b64 s[96:97], exec, s[20:21]
	s_andn2_b64 vcc, exec, s[20:21]
	v_mov_b32_e32 v81, 0
	s_nop 0
	v_mov_b32_e32 v82, 0
	v_mov_b32_e32 v83, 0
	s_cbranch_vccnz .LBB0_5092
	ds_read_b128 v[80:83], v187 offset:21760
	ds_read_b128 v[84:87], v187 offset:21824
	ds_read_b128 v[202:205], v187 offset:21888
	ds_read_b128 v[206:209], v187 offset:21952
	s_waitcnt lgkmcnt(3)
	v_mfma_f32_16x16x32_f16 v[80:83], v[80:83], v[66:69], 0
	s_waitcnt lgkmcnt(2)
	v_mfma_f32_16x16x32_f16 v[80:83], v[84:87], v[46:49], v[80:83]
	s_waitcnt lgkmcnt(1)
	v_mfma_f32_16x16x32_f16 v[80:83], v[202:205], v[42:45], v[80:83]
	s_waitcnt lgkmcnt(0)
	v_mfma_f32_16x16x32_f16 v[80:83], v[206:209], v[38:41], v[80:83]
.LBB0_5092:
	v_mov_b32_e32 v84, 0
	s_andn2_b64 s[92:93], exec, s[22:23]
	s_andn2_b64 vcc, exec, s[22:23]
	v_mov_b32_e32 v88, 0
	v_mov_b32_e32 v89, 0
	v_mov_b32_e32 v90, 0
	v_mov_b32_e32 v91, 0
	s_cbranch_vccnz .LBB0_5094
	ds_read_b128 v[86:89], v187 offset:26112
	ds_read_b128 v[192:195], v187 offset:26176
	ds_read_b128 v[202:205], v187 offset:26240
	ds_read_b128 v[206:209], v187 offset:26304
	s_waitcnt lgkmcnt(3)
	v_mfma_f32_16x16x32_f16 v[86:89], v[86:89], v[66:69], 0
	s_waitcnt lgkmcnt(2)
	v_mfma_f32_16x16x32_f16 v[86:89], v[192:195], v[46:49], v[86:89]
	s_waitcnt lgkmcnt(1)
	v_mfma_f32_16x16x32_f16 v[86:89], v[202:205], v[42:45], v[86:89]
	s_waitcnt lgkmcnt(0)
	v_mfma_f32_16x16x32_f16 v[88:91], v[206:209], v[38:41], v[86:89]
.LBB0_5094:
	s_andn2_b64 s[94:95], exec, s[24:25]
	s_andn2_b64 vcc, exec, s[24:25]
	v_mov_b32_e32 v85, 0
	s_nop 0
	v_mov_b32_e32 v86, 0
	v_mov_b32_e32 v87, 0
	s_cbranch_vccnz .LBB0_5096
	ds_read_b128 v[84:87], v187 offset:30464
	ds_read_b128 v[192:195], v187 offset:30528
	ds_read_b128 v[202:205], v187 offset:30592
	ds_read_b128 v[206:209], v187 offset:30656
	s_waitcnt lgkmcnt(3)
	v_mfma_f32_16x16x32_f16 v[84:87], v[84:87], v[66:69], 0
	s_waitcnt lgkmcnt(2)
	v_mfma_f32_16x16x32_f16 v[84:87], v[192:195], v[46:49], v[84:87]
	s_waitcnt lgkmcnt(1)
	v_mfma_f32_16x16x32_f16 v[84:87], v[202:205], v[42:45], v[84:87]
	s_waitcnt lgkmcnt(0)
	v_mfma_f32_16x16x32_f16 v[84:87], v[206:209], v[38:41], v[84:87]
.LBB0_5096:
	v_lshl_add_u32 v137, v147, 2, s81
	ds_read_b32 v139, v137 offset:62720
	v_lshl_add_u32 v192, v118, 2, s81
	s_mov_b64 s[36:37], -1
	s_and_b64 vcc, exec, s[82:83]
	s_cbranch_vccz .LBB0_5113
	ds_read_b128 v[194:197], v192 offset:62208
	v_cmp_gt_i32_e64 s[36:37], 0, v244
	s_waitcnt lgkmcnt(0)
	v_sub_f32_e32 v70, v194, v139
	v_sub_f32_e32 v71, v195, v139
	v_mul_f32_e32 v70, 0x3fb8aa3b, v70
	v_mul_f32_e32 v71, 0x3fb8aa3b, v71
	v_exp_f32_e32 v70, v70
	v_exp_f32_e32 v71, v71
	v_sub_f32_e32 v193, v196, v139
	v_mul_f32_e32 v193, 0x3fb8aa3b, v193
	v_fma_mixlo_f16 v70, v100, v70, 0
	v_fma_mixlo_f16 v71, v101, v71, 0
	v_exp_f32_e32 v100, v193
	v_sub_f32_e32 v101, v197, v139
	v_cndmask_b32_e64 v70, v70, 0, s[36:37]
	v_mul_f32_e32 v101, 0x3fb8aa3b, v101
	v_cmp_lt_i32_e64 s[36:37], 0, v244
	v_exp_f32_e32 v101, v101
	s_nop 0
	v_cndmask_b32_e64 v71, 0, v71, s[36:37]
	v_pack_b32_f16 v70, v70, v71
	v_fma_mixlo_f16 v71, v102, v100, 0
	v_cmp_gt_i32_e64 s[36:37], 2, v244
	v_fma_mixlo_f16 v100, v103, v101, 0
	s_nop 0
	v_cndmask_b32_e64 v71, v71, 0, s[36:37]
	v_cmp_gt_i32_e64 s[36:37], 3, v244
	s_nop 1
	v_cndmask_b32_e64 v100, v100, 0, s[36:37]
	v_pack_b32_f16 v71, v71, v100
	s_cbranch_execz .LBB0_5114
